# s12 + x1: U chunk-state stores write-through (sc1): consumers (x2) sit on other XCDs anyway
# baseline (speedup 1.0000x reference)
; __device__ __forceinline__ int crow(int r, int hi) { return (r & 3) + 8 * (r >> 2) + 4 * hi; }
; __device__ __forceinline__ int crow(int r, int hi) { return (r & 3) + 8 * (r >> 2) + 4 * hi; }
; #define MF32(a, b, c) __builtin_amdgcn_mfma_f32_32x32x16_f16(__builtin_bit_cast(h16x8, (a)), __builtin_bit_cast(h16x8, (b)), (c), 0, 0, 0)
; __device__ __forceinline__ void x1_wave(int item, int b0, const h16* __restrict__ proj, const float* __restrict__ small, const float* __restrict__ convw, ...
;     ...
;     const int lb = ((lane >> 4) & 1) * 32 + (lane & 3) * 8 + (4 * hi + ((lane & 15) >> 2)) * 64;
;     h16* up = U + ((size_t)lbh * 32 + c) * 8192;
; #pragma unroll 1
;     for (int vb = 0; vb < 4; ++vb) {
;         f32x16 a0 = f32x16{}, a1 = f32x16{};
; #pragma unroll
;         for (int ks = 0; ks < 4; ++ks) { const s16x8 vf = trfrag((lds_cptr)(R + W_V), vb, ks, lb);
;             a0 = MF32(vf, trfrag((lds_cptr)(R + W_K), 0, ks, lb), a0); a1 = MF32(vf, trfrag((lds_cptr)(R + W_K), 1, ks, lb), a1); }
; #pragma unroll
;         for (int r = 0; r < 16; ++r) { up[(vb * 32 + crow(r, hi)) * 64 + r32] = (h16)a0[r]; up[(vb * 32 + crow(r, hi)) * 64 + 32 + r32] = (h16)a1[r]; }
;     }
.LBB0_917:
	v_add_u32_e32 v46, v35, v34
	ds_read_b64_tr_b16 v[16:17], v46
	ds_read_b64_tr_b16 v[18:19], v46 offset:512
	ds_read_b64_tr_b16 v[0:1], v36 offset:16384
	ds_read_b64_tr_b16 v[2:3], v36 offset:16896
	ds_read_b64_tr_b16 v[20:21], v36 offset:20480
	ds_read_b64_tr_b16 v[22:23], v36 offset:20992
	ds_read_b64_tr_b16 v[38:39], v46 offset:1024
	ds_read_b64_tr_b16 v[40:41], v46 offset:1536
	ds_read_b64_tr_b16 v[42:43], v36 offset:17408
	ds_read_b64_tr_b16 v[44:45], v36 offset:17920
	s_add_i32 s13, s13, -1
	v_add_u32_e32 v35, 0x1000, v35
	s_waitcnt lgkmcnt(6)
	v_mfma_f32_32x32x16_f16 v[0:15], v[0:3], v[16:19], 0
	s_cmp_lg_u32 s13, 0
	s_waitcnt lgkmcnt(4)
	v_mfma_f32_32x32x16_f16 v[16:31], v[20:23], v[16:19], 0
	s_waitcnt lgkmcnt(0)
	v_mfma_f32_32x32x16_f16 v[0:15], v[42:45], v[38:41], v[0:15]
	ds_read_b64_tr_b16 v[42:43], v36 offset:21504
	ds_read_b64_tr_b16 v[44:45], v36 offset:22016
	s_waitcnt lgkmcnt(0)
	v_mfma_f32_32x32x16_f16 v[16:31], v[42:45], v[38:41], v[16:31]
	ds_read_b64_tr_b16 v[38:39], v46 offset:2048
	ds_read_b64_tr_b16 v[40:41], v46 offset:2560
	ds_read_b64_tr_b16 v[42:43], v36 offset:18432
	ds_read_b64_tr_b16 v[44:45], v36 offset:18944
	s_waitcnt lgkmcnt(0)
	v_mfma_f32_32x32x16_f16 v[0:15], v[42:45], v[38:41], v[0:15]
	ds_read_b64_tr_b16 v[42:43], v36 offset:22528
	ds_read_b64_tr_b16 v[44:45], v36 offset:23040
	s_waitcnt lgkmcnt(0)
	v_mfma_f32_32x32x16_f16 v[16:31], v[42:45], v[38:41], v[16:31]
	ds_read_b64_tr_b16 v[38:39], v46 offset:3072
	ds_read_b64_tr_b16 v[40:41], v46 offset:3584
	ds_read_b64_tr_b16 v[42:43], v36 offset:19456
	ds_read_b64_tr_b16 v[44:45], v36 offset:19968
	s_waitcnt lgkmcnt(0)
	v_mfma_f32_32x32x16_f16 v[0:15], v[42:45], v[38:41], v[0:15]
	ds_read_b64_tr_b16 v[42:43], v36 offset:23552
	ds_read_b64_tr_b16 v[44:45], v36 offset:24064
	s_waitcnt lgkmcnt(0)
	v_mfma_f32_32x32x16_f16 v[16:31], v[42:45], v[38:41], v[16:31]
	s_nop 7
	s_nop 7
	v_cvt_pk_f16_f32 v0, v0, v1
	v_cvt_pk_f16_f32 v1, v2, v3
	v_cvt_pk_f16_f32 v2, v8, v9
	v_cvt_pk_f16_f32 v3, v10, v11
	v_cvt_pk_f16_f32 v4, v4, v5
	v_cvt_pk_f16_f32 v5, v6, v7
	v_cvt_pk_f16_f32 v6, v12, v13
	v_cvt_pk_f16_f32 v7, v14, v15
	v_cvt_pk_f16_f32 v16, v16, v17
	v_cvt_pk_f16_f32 v17, v18, v19
	v_cvt_pk_f16_f32 v18, v24, v25
	v_cvt_pk_f16_f32 v19, v26, v27
	v_cvt_pk_f16_f32 v20, v20, v21
	v_cvt_pk_f16_f32 v21, v22, v23
	v_cvt_pk_f16_f32 v22, v28, v29
	v_cvt_pk_f16_f32 v23, v30, v31
	v_ashrrev_i32_e32 v39, 31, v37
	v_mov_b32_e32 v38, v37
	v_permlane32_swap_b32_e32 v0, v2
	v_permlane32_swap_b32_e32 v1, v3
	v_permlane32_swap_b32_e32 v4, v6
	v_permlane32_swap_b32_e32 v5, v7
	v_permlane32_swap_b32_e32 v16, v18
	v_permlane32_swap_b32_e32 v17, v19
	v_permlane32_swap_b32_e32 v20, v22
	v_permlane32_swap_b32_e32 v21, v23
	v_lshl_add_u64 v[38:39], v[38:39], 1, s[0:1]
	v_add_u32_e32 v37, 0x800, v37
	s_nop 1
	global_store_dwordx4 v[38:39], v[0:3], off sc1
	global_store_dwordx4 v[38:39], v[4:7], off offset:16 sc1
	global_store_dwordx4 v[38:39], v[16:19], off offset:64 sc1
	global_store_dwordx4 v[38:39], v[20:23], off offset:80 sc1
	s_cbranch_scc1 .LBB0_917
	v_lshlrev_b32_e32 v0, 1, v32
	v_lshl_or_b32 v0, v33, 12, v0
	v_add_u32_e32 v0, s11, v0
	v_mov_b32_e32 v1, 0
	s_mov_b32 s0, 0
